# v118 + CONVE: first inner iteration peeled, each batch's 8 output stores deferred until after the next batch's 16 loads are issued (vmcnt thresholds +8)
# speedup vs baseline: 1.0064x; 1.0064x over previous
; __device__ __forceinline__ f32x4 bf4lo(const v4u& w) { return (f32x4){bflo(w.x), bfhi(w.x), bflo(w.y), bfhi(w.y)}; }
; __device__ __forceinline__ f32x4 bf4hi(const v4u& w) { return (f32x4){bflo(w.z), bfhi(w.z), bflo(w.w), bfhi(w.w)}; }
; __device__ __forceinline__ void ph_conv(Frame& F) {
;     ...
;         for (int tb = 0; tb < 32; tb += 8) {
;             v4u uu[8], bb[8];
; #pragma unroll
;             for (int j = 0; j < 8; ++j) { const size_t off = (size_t)(t0 + tb + j) * D + c; uu[j] = __builtin_nontemporal_load((const v4u*)(U + off)); bb[j] = __builtin_nontemporal_load((const v4u*)(BG + off)); }
; #pragma unroll
;             for (int j = 0; j < 8; ++j) {
;                 const f32x4 u0l = bf4lo(uu[j]), u0h = bf4hi(uu[j]), bl = bf4lo(bb[j]), bh = bf4hi(bb[j]);
;                 const f32x4 yl = bl * (wa0 * u2l + wb0 * u1l + wc0 * u0l), yh = bh * (wa1 * u2h + wb1 * u1h + wc1 * u0h);
.LBB0_1128:
	v_add_u32_e32 v34, s16, v64
	v_add_u32_e32 v56, 8, v34
	v_add_u32_e32 v58, 9, v34
	v_add_u32_e32 v60, 10, v34
	v_add_u32_e32 v62, 11, v34
	v_add_u32_e32 v66, 12, v34
	v_add_u32_e32 v68, 13, v34
	v_add_u32_e32 v70, 14, v34
	v_add_u32_e32 v72, 15, v34
	v_pk_mul_f32 v[48:49], v[12:13], v[28:29]
	v_pk_mul_f32 v[50:51], v[10:11], v[26:27]
	v_pk_mul_f32 v[52:53], v[20:21], v[32:33]
	v_pk_mul_f32 v[54:55], v[18:19], v[30:31]
	v_ashrrev_i32_e32 v57, 31, v56
	v_ashrrev_i32_e32 v59, 31, v58
	v_ashrrev_i32_e32 v61, 31, v60
	v_ashrrev_i32_e32 v63, 31, v62
	v_ashrrev_i32_e32 v67, 31, v66
	v_ashrrev_i32_e32 v69, 31, v68
	v_ashrrev_i32_e32 v71, 31, v70
	v_ashrrev_i32_e32 v73, 31, v72
	v_pk_fma_f32 v[122:123], v[8:9], v[42:43], v[48:49]
	v_pk_fma_f32 v[124:125], v[6:7], v[40:41], v[50:51]
	v_pk_fma_f32 v[126:127], v[4:5], v[46:47], v[52:53]
	v_pk_fma_f32 v[128:129], v[2:3], v[44:45], v[54:55]
	v_lshlrev_b64 v[40:41], 12, v[56:57]
	v_lshlrev_b64 v[42:43], 12, v[58:59]
	v_lshlrev_b64 v[44:45], 12, v[60:61]
	v_lshlrev_b64 v[46:47], 12, v[62:63]
	v_lshlrev_b64 v[54:55], 12, v[66:67]
	v_lshlrev_b64 v[56:57], 12, v[68:69]
	v_lshlrev_b64 v[58:59], 12, v[70:71]
	v_lshlrev_b64 v[60:61], 12, v[72:73]
	v_or_b32_e32 v66, v40, v65
	v_mov_b32_e32 v67, v41
	v_or_b32_e32 v68, v42, v65
	v_mov_b32_e32 v69, v43
	v_or_b32_e32 v70, v44, v65
	v_mov_b32_e32 v71, v45
	v_or_b32_e32 v72, v46, v65
	v_mov_b32_e32 v73, v47
	v_or_b32_e32 v74, v54, v65
	v_mov_b32_e32 v75, v55
	v_or_b32_e32 v76, v56, v65
	v_mov_b32_e32 v77, v57
	v_or_b32_e32 v78, v58, v65
	v_mov_b32_e32 v79, v59
	v_or_b32_e32 v80, v60, v65
	v_mov_b32_e32 v81, v61
	v_lshl_add_u64 v[86:87], s[14:15], 0, v[66:67]
	v_lshl_add_u64 v[88:89], s[10:11], 0, v[66:67]
	v_lshl_add_u64 v[90:91], s[14:15], 0, v[68:69]
	v_lshl_add_u64 v[92:93], s[10:11], 0, v[68:69]
	v_lshl_add_u64 v[94:95], s[14:15], 0, v[70:71]
	v_lshl_add_u64 v[96:97], s[10:11], 0, v[70:71]
	v_lshl_add_u64 v[98:99], s[14:15], 0, v[72:73]
	v_lshl_add_u64 v[102:103], s[10:11], 0, v[72:73]
	v_lshl_add_u64 v[104:105], s[14:15], 0, v[74:75]
	v_lshl_add_u64 v[106:107], s[10:11], 0, v[74:75]
	v_lshl_add_u64 v[108:109], s[14:15], 0, v[76:77]
	v_lshl_add_u64 v[110:111], s[10:11], 0, v[76:77]
	v_lshl_add_u64 v[112:113], s[14:15], 0, v[78:79]
	v_lshl_add_u64 v[114:115], s[10:11], 0, v[78:79]
	v_lshl_add_u64 v[116:117], s[14:15], 0, v[80:81]
	v_lshl_add_u64 v[118:119], s[10:11], 0, v[80:81]
	v_lshl_add_u64 v[62:63], v[38:39], 0, v[40:41]
	v_lshl_add_u64 v[48:49], v[38:39], 0, v[42:43]
	v_lshl_add_u64 v[50:51], v[38:39], 0, v[44:45]
	v_lshl_add_u64 v[52:53], v[38:39], 0, v[46:47]
	global_load_dwordx4 v[40:43], v[86:87], off nt
	global_load_dwordx4 v[44:47], v[88:89], off nt
	global_load_dwordx4 v[66:69], v[90:91], off nt
	global_load_dwordx4 v[70:73], v[92:93], off nt
	global_load_dwordx4 v[74:77], v[94:95], off nt
	global_load_dwordx4 v[78:81], v[96:97], off nt
	global_load_dwordx4 v[82:85], v[98:99], off nt
	global_load_dwordx4 v[86:89], v[102:103], off nt
	s_nop 0
	global_load_dwordx4 v[90:93], v[104:105], off nt
	global_load_dwordx4 v[94:97], v[106:107], off nt
	global_load_dwordx4 v[98:101], v[108:109], off nt
	s_nop 0
	global_load_dwordx4 v[102:105], v[110:111], off nt
	global_load_dwordx4 v[106:109], v[112:113], off nt
	s_nop 0
	global_load_dwordx4 v[110:113], v[114:115], off nt
	s_nop 0
	global_load_dwordx4 v[114:117], v[116:117], off nt
	s_nop 0
	global_load_dwordx4 v[118:121], v[118:119], off nt
	s_add_i32 s16, s16, 8
	s_cmp_gt_u32 s16, 23
	v_lshl_add_u64 v[54:55], v[38:39], 0, v[54:55]
	v_lshl_add_u64 v[56:57], v[38:39], 0, v[56:57]
	v_lshl_add_u64 v[58:59], v[38:39], 0, v[58:59]
	v_lshl_add_u64 v[60:61], v[38:39], 0, v[60:61]
	s_waitcnt vmcnt(15)
	v_lshlrev_b32_e32 v130, 16, v40
	v_and_b32_e32 v131, 0xffff0000, v40
	v_lshlrev_b32_e32 v132, 16, v41
	v_and_b32_e32 v133, 0xffff0000, v41
	v_lshlrev_b32_e32 v134, 16, v42
	v_and_b32_e32 v135, 0xffff0000, v42
	v_lshlrev_b32_e32 v136, 16, v43
	v_and_b32_e32 v137, 0xffff0000, v43
	s_waitcnt vmcnt(14)
	v_lshlrev_b32_e32 v138, 16, v44
	v_and_b32_e32 v139, 0xffff0000, v44
	v_lshlrev_b32_e32 v140, 16, v45
	v_and_b32_e32 v141, 0xffff0000, v45
	v_lshlrev_b32_e32 v142, 16, v46
	v_and_b32_e32 v143, 0xffff0000, v46
	v_lshlrev_b32_e32 v144, 16, v47
	v_and_b32_e32 v145, 0xffff0000, v47
	s_waitcnt vmcnt(13)
	v_lshlrev_b32_e32 v146, 16, v66
	v_and_b32_e32 v147, 0xffff0000, v66
	v_lshlrev_b32_e32 v66, 16, v67
	v_and_b32_e32 v67, 0xffff0000, v67
	v_lshlrev_b32_e32 v148, 16, v68
	v_and_b32_e32 v149, 0xffff0000, v68
	v_lshlrev_b32_e32 v68, 16, v69
	v_and_b32_e32 v69, 0xffff0000, v69
	s_waitcnt vmcnt(11)
	v_lshlrev_b32_e32 v154, 16, v74
	v_and_b32_e32 v155, 0xffff0000, v74
	v_lshlrev_b32_e32 v74, 16, v75
	v_and_b32_e32 v75, 0xffff0000, v75
	v_lshlrev_b32_e32 v156, 16, v76
	v_and_b32_e32 v157, 0xffff0000, v76
	v_lshlrev_b32_e32 v76, 16, v77
	v_and_b32_e32 v77, 0xffff0000, v77
	s_waitcnt vmcnt(9)
	v_lshlrev_b32_e32 v162, 16, v82
	v_and_b32_e32 v163, 0xffff0000, v82
	v_lshlrev_b32_e32 v82, 16, v83
	v_and_b32_e32 v83, 0xffff0000, v83
	v_lshlrev_b32_e32 v164, 16, v84
	v_and_b32_e32 v165, 0xffff0000, v84
	v_lshlrev_b32_e32 v84, 16, v85
	v_and_b32_e32 v85, 0xffff0000, v85
	s_waitcnt vmcnt(7)
	v_lshlrev_b32_e32 v170, 16, v90
	v_and_b32_e32 v171, 0xffff0000, v90
	v_lshlrev_b32_e32 v90, 16, v91
	v_and_b32_e32 v91, 0xffff0000, v91
	v_lshlrev_b32_e32 v172, 16, v92
	v_and_b32_e32 v173, 0xffff0000, v92
	v_lshlrev_b32_e32 v92, 16, v93
	v_and_b32_e32 v93, 0xffff0000, v93
	s_waitcnt vmcnt(5)
	v_lshlrev_b32_e32 v178, 16, v98
	v_and_b32_e32 v179, 0xffff0000, v98
	v_lshlrev_b32_e32 v98, 16, v99
	v_and_b32_e32 v99, 0xffff0000, v99
	v_lshlrev_b32_e32 v180, 16, v100
	v_and_b32_e32 v181, 0xffff0000, v100
	v_lshlrev_b32_e32 v100, 16, v101
	v_and_b32_e32 v101, 0xffff0000, v101
	s_waitcnt vmcnt(3)
; __device__ __forceinline__ f32x4 bf4lo(const v4u& w) { return (f32x4){bflo(w.x), bfhi(w.x), bflo(w.y), bfhi(w.y)}; }
; __device__ __forceinline__ f32x4 bf4hi(const v4u& w) { return (f32x4){bflo(w.z), bfhi(w.z), bflo(w.w), bfhi(w.w)}; }
; __device__ __forceinline__ void ph_conv(Frame& F) {
;     ...
;             for (int j = 0; j < 8; ++j) {
;                 const f32x4 u0l = bf4lo(uu[j]), u0h = bf4hi(uu[j]), bl = bf4lo(bb[j]), bh = bf4hi(bb[j]);
;                 const f32x4 yl = bl * (wa0 * u2l + wb0 * u1l + wc0 * u0l), yh = bh * (wa1 * u2h + wb1 * u1h + wc1 * u0h);
	v_lshlrev_b32_e32 v40, 16, v106
	v_and_b32_e32 v41, 0xffff0000, v106
	v_lshlrev_b32_e32 v42, 16, v107
	v_and_b32_e32 v43, 0xffff0000, v107
	v_lshlrev_b32_e32 v44, 16, v108
	v_and_b32_e32 v45, 0xffff0000, v108
	v_lshlrev_b32_e32 v46, 16, v109
	v_and_b32_e32 v47, 0xffff0000, v109
	v_pk_fma_f32 v[124:125], v[14:15], v[130:131], v[124:125]
	v_pk_fma_f32 v[122:123], v[16:17], v[132:133], v[122:123]
	v_pk_fma_f32 v[128:129], v[22:23], v[134:135], v[128:129]
	v_pk_fma_f32 v[126:127], v[24:25], v[136:137], v[126:127]
	v_pk_mul_f32 v[190:191], v[10:11], v[130:131]
	v_pk_mul_f32 v[192:193], v[12:13], v[132:133]
	v_pk_mul_f32 v[194:195], v[18:19], v[134:135]
	v_pk_mul_f32 v[196:197], v[20:21], v[136:137]
	v_pk_mul_f32 v[198:199], v[10:11], v[146:147]
	v_pk_mul_f32 v[200:201], v[12:13], v[66:67]
	v_pk_mul_f32 v[202:203], v[18:19], v[148:149]
	v_pk_mul_f32 v[204:205], v[20:21], v[68:69]
	v_pk_mul_f32 v[206:207], v[10:11], v[154:155]
	v_pk_mul_f32 v[208:209], v[12:13], v[74:75]
	v_pk_mul_f32 v[210:211], v[18:19], v[156:157]
	v_pk_mul_f32 v[212:213], v[20:21], v[76:77]
	v_pk_mul_f32 v[214:215], v[10:11], v[162:163]
	v_pk_mul_f32 v[216:217], v[12:13], v[82:83]
	v_pk_mul_f32 v[218:219], v[18:19], v[164:165]
	v_pk_mul_f32 v[220:221], v[20:21], v[84:85]
	v_pk_mul_f32 v[222:223], v[10:11], v[170:171]
	v_pk_mul_f32 v[224:225], v[12:13], v[90:91]
	v_pk_mul_f32 v[226:227], v[18:19], v[172:173]
	v_pk_mul_f32 v[228:229], v[20:21], v[92:93]
	v_pk_mul_f32 v[230:231], v[10:11], v[178:179]
	v_pk_mul_f32 v[232:233], v[12:13], v[98:99]
	v_pk_mul_f32 v[234:235], v[18:19], v[180:181]
	v_pk_mul_f32 v[236:237], v[20:21], v[100:101]
	v_pk_mul_f32 v[238:239], v[10:11], v[40:41]
	v_pk_mul_f32 v[240:241], v[12:13], v[42:43]
	v_pk_mul_f32 v[242:243], v[18:19], v[44:45]
	v_pk_mul_f32 v[244:245], v[20:21], v[46:47]
	v_pk_mul_f32 v[122:123], v[122:123], v[140:141]
	v_pk_mul_f32 v[124:125], v[124:125], v[138:139]
	v_pk_mul_f32 v[126:127], v[126:127], v[144:145]
	v_pk_mul_f32 v[128:129], v[128:129], v[142:143]
	v_pk_fma_f32 v[138:139], v[8:9], v[28:29], v[192:193]
	v_pk_fma_f32 v[140:141], v[6:7], v[26:27], v[190:191]
	v_pk_fma_f32 v[142:143], v[4:5], v[32:33], v[196:197]
	v_pk_fma_f32 v[144:145], v[2:3], v[30:31], v[194:195]
	v_lshlrev_b32_e32 v150, 16, v70
	v_and_b32_e32 v151, 0xffff0000, v70
	v_lshlrev_b32_e32 v70, 16, v71
	v_and_b32_e32 v71, 0xffff0000, v71
	v_lshlrev_b32_e32 v152, 16, v72
	v_and_b32_e32 v153, 0xffff0000, v72
	v_lshlrev_b32_e32 v72, 16, v73
	v_and_b32_e32 v73, 0xffff0000, v73
	v_pk_fma_f32 v[132:133], v[8:9], v[132:133], v[200:201]
	v_pk_fma_f32 v[130:131], v[6:7], v[130:131], v[198:199]
	v_pk_fma_f32 v[136:137], v[4:5], v[136:137], v[204:205]
	v_pk_fma_f32 v[134:135], v[2:3], v[134:135], v[202:203]
	v_pk_fma_f32 v[190:191], v[8:9], v[66:67], v[208:209]
	v_pk_fma_f32 v[192:193], v[6:7], v[146:147], v[206:207]
	v_pk_fma_f32 v[194:195], v[4:5], v[68:69], v[212:213]
	v_pk_fma_f32 v[196:197], v[2:3], v[148:149], v[210:211]
	v_pk_fma_f32 v[198:199], v[8:9], v[74:75], v[216:217]
	v_pk_fma_f32 v[200:201], v[6:7], v[154:155], v[214:215]
	v_pk_fma_f32 v[202:203], v[4:5], v[76:77], v[220:221]
	v_pk_fma_f32 v[204:205], v[2:3], v[156:157], v[218:219]
	v_pk_fma_f32 v[206:207], v[8:9], v[82:83], v[224:225]
	v_pk_fma_f32 v[208:209], v[6:7], v[162:163], v[222:223]
	v_pk_fma_f32 v[210:211], v[4:5], v[84:85], v[228:229]
	v_pk_fma_f32 v[212:213], v[2:3], v[164:165], v[226:227]
	v_pk_fma_f32 v[214:215], v[8:9], v[90:91], v[232:233]
	v_pk_fma_f32 v[216:217], v[6:7], v[170:171], v[230:231]
	v_pk_fma_f32 v[218:219], v[4:5], v[92:93], v[236:237]
	v_pk_fma_f32 v[220:221], v[2:3], v[172:173], v[234:235]
	s_waitcnt vmcnt(1)
	v_lshlrev_b32_e32 v26, 16, v114
	v_and_b32_e32 v27, 0xffff0000, v114
	v_lshlrev_b32_e32 v28, 16, v115
	v_and_b32_e32 v29, 0xffff0000, v115
	v_lshlrev_b32_e32 v30, 16, v116
	v_and_b32_e32 v31, 0xffff0000, v116
	v_lshlrev_b32_e32 v32, 16, v117
	v_and_b32_e32 v33, 0xffff0000, v117
	v_pk_fma_f32 v[114:115], v[8:9], v[98:99], v[240:241]
	v_pk_fma_f32 v[116:117], v[6:7], v[178:179], v[238:239]
	v_pk_fma_f32 v[222:223], v[4:5], v[100:101], v[244:245]
	v_pk_fma_f32 v[224:225], v[2:3], v[180:181], v[242:243]
	v_bfe_u32 v34, v124, 16, 1
	v_bfe_u32 v226, v125, 16, 1
	v_bfe_u32 v227, v122, 16, 1
	v_bfe_u32 v228, v123, 16, 1
	v_bfe_u32 v229, v128, 16, 1
	v_bfe_u32 v231, v126, 16, 1
	v_pk_fma_f32 v[140:141], v[14:15], v[146:147], v[140:141]
	v_pk_fma_f32 v[66:67], v[16:17], v[66:67], v[138:139]
	v_pk_fma_f32 v[138:139], v[22:23], v[148:149], v[144:145]
	v_pk_fma_f32 v[68:69], v[24:25], v[68:69], v[142:143]
	v_lshlrev_b32_e32 v158, 16, v78
	v_and_b32_e32 v159, 0xffff0000, v78
	v_lshlrev_b32_e32 v78, 16, v79
	v_and_b32_e32 v79, 0xffff0000, v79
	v_lshlrev_b32_e32 v160, 16, v80
	v_and_b32_e32 v161, 0xffff0000, v80
	v_lshlrev_b32_e32 v80, 16, v81
	v_and_b32_e32 v81, 0xffff0000, v81
	v_lshlrev_b32_e32 v166, 16, v86
	v_and_b32_e32 v167, 0xffff0000, v86
	v_lshlrev_b32_e32 v86, 16, v87
	v_and_b32_e32 v87, 0xffff0000, v87
	v_lshlrev_b32_e32 v168, 16, v88
	v_and_b32_e32 v169, 0xffff0000, v88
	v_lshlrev_b32_e32 v88, 16, v89
	v_and_b32_e32 v89, 0xffff0000, v89
	v_lshlrev_b32_e32 v174, 16, v94
	v_and_b32_e32 v175, 0xffff0000, v94
	v_lshlrev_b32_e32 v94, 16, v95
	v_and_b32_e32 v95, 0xffff0000, v95
	v_lshlrev_b32_e32 v176, 16, v96
	v_and_b32_e32 v177, 0xffff0000, v96
	v_lshlrev_b32_e32 v96, 16, v97
	v_and_b32_e32 v97, 0xffff0000, v97
	v_lshlrev_b32_e32 v182, 16, v102
	v_and_b32_e32 v183, 0xffff0000, v102
	v_lshlrev_b32_e32 v102, 16, v103
	v_and_b32_e32 v103, 0xffff0000, v103
	v_lshlrev_b32_e32 v184, 16, v104
	v_and_b32_e32 v185, 0xffff0000, v104
	v_lshlrev_b32_e32 v104, 16, v105
	v_and_b32_e32 v105, 0xffff0000, v105
	v_lshlrev_b32_e32 v106, 16, v110
	v_and_b32_e32 v107, 0xffff0000, v110
	v_lshlrev_b32_e32 v108, 16, v111
	v_and_b32_e32 v109, 0xffff0000, v111
	v_lshlrev_b32_e32 v110, 16, v112
	v_and_b32_e32 v111, 0xffff0000, v112
	v_lshlrev_b32_e32 v112, 16, v113
	v_and_b32_e32 v113, 0xffff0000, v113
	s_waitcnt vmcnt(0)
; __device__ __forceinline__ f32x4 bf4lo(const v4u& w) { return (f32x4){bflo(w.x), bfhi(w.x), bflo(w.y), bfhi(w.y)}; }
; __device__ __forceinline__ f32x4 bf4hi(const v4u& w) { return (f32x4){bflo(w.z), bfhi(w.z), bflo(w.w), bfhi(w.w)}; }
; __device__ __forceinline__ unsigned f2bf(float f) { unsigned u = __builtin_bit_cast(unsigned, f); return (u + 0x7fffu + ((u >> 16) & 1u)) >> 16; }
; __device__ __forceinline__ unsigned pk2(float lo, float hi) { return f2bf(lo) | (f2bf(hi) << 16); }
; __device__ __forceinline__ void ph_conv(Frame& F) {
;     ...
;             for (int j = 0; j < 8; ++j) {
;                 const f32x4 u0l = bf4lo(uu[j]), u0h = bf4hi(uu[j]), bl = bf4lo(bb[j]), bh = bf4hi(bb[j]);
;                 const f32x4 yl = bl * (wa0 * u2l + wb0 * u1l + wc0 * u0l), yh = bh * (wa1 * u2h + wb1 * u1h + wc1 * u0h);
;                 v4u o; o.x = pk2(yl.x, yl.y); o.y = pk2(yl.z, yl.w); o.z = pk2(yh.x, yh.y); o.w = pk2(yh.z, yh.w);
	v_lshlrev_b32_e32 v186, 16, v118
	v_and_b32_e32 v187, 0xffff0000, v118
	v_lshlrev_b32_e32 v118, 16, v119
	v_and_b32_e32 v119, 0xffff0000, v119
	v_lshlrev_b32_e32 v188, 16, v120
	v_and_b32_e32 v189, 0xffff0000, v120
	v_lshlrev_b32_e32 v120, 16, v121
	v_and_b32_e32 v121, 0xffff0000, v121
	v_bfe_u32 v230, v129, 16, 1
	v_bfe_u32 v232, v127, 16, 1
	v_pk_fma_f32 v[130:131], v[14:15], v[154:155], v[130:131]
	v_pk_fma_f32 v[74:75], v[16:17], v[74:75], v[132:133]
	v_pk_fma_f32 v[132:133], v[22:23], v[156:157], v[134:135]
	v_pk_fma_f32 v[76:77], v[24:25], v[76:77], v[136:137]
	v_pk_fma_f32 v[134:135], v[14:15], v[162:163], v[192:193]
	v_pk_fma_f32 v[82:83], v[16:17], v[82:83], v[190:191]
	v_pk_fma_f32 v[136:137], v[22:23], v[164:165], v[196:197]
	v_pk_fma_f32 v[84:85], v[24:25], v[84:85], v[194:195]
	v_pk_fma_f32 v[142:143], v[14:15], v[170:171], v[200:201]
	v_pk_fma_f32 v[90:91], v[16:17], v[90:91], v[198:199]
	v_pk_fma_f32 v[144:145], v[22:23], v[172:173], v[204:205]
	v_pk_fma_f32 v[92:93], v[24:25], v[92:93], v[202:203]
	v_pk_fma_f32 v[146:147], v[14:15], v[178:179], v[208:209]
	v_pk_fma_f32 v[98:99], v[16:17], v[98:99], v[206:207]
	v_pk_fma_f32 v[148:149], v[22:23], v[180:181], v[212:213]
	v_pk_fma_f32 v[100:101], v[24:25], v[100:101], v[210:211]
	v_pk_fma_f32 v[154:155], v[14:15], v[40:41], v[216:217]
	v_pk_fma_f32 v[156:157], v[16:17], v[42:43], v[214:215]
	v_pk_fma_f32 v[162:163], v[22:23], v[44:45], v[220:221]
	v_pk_fma_f32 v[164:165], v[24:25], v[46:47], v[218:219]
	v_pk_fma_f32 v[116:117], v[14:15], v[26:27], v[116:117]
	v_pk_fma_f32 v[114:115], v[16:17], v[28:29], v[114:115]
	v_pk_fma_f32 v[170:171], v[22:23], v[30:31], v[224:225]
	v_pk_fma_f32 v[172:173], v[24:25], v[32:33], v[222:223]
	v_add3_u32 v34, v124, v34, s19
	v_add3_u32 v178, v125, v226, s19
	v_add3_u32 v179, v122, v227, s19
	v_add3_u32 v180, v123, v228, s19
	v_add3_u32 v128, v128, v229, s19
	v_add3_u32 v126, v126, v231, s19
	v_pk_mul_f32 v[70:71], v[66:67], v[70:71]
	v_pk_mul_f32 v[122:123], v[140:141], v[150:151]
	v_pk_mul_f32 v[72:73], v[68:69], v[72:73]
	v_pk_mul_f32 v[124:125], v[138:139], v[152:153]
	v_add3_u32 v129, v129, v230, s19
	v_add3_u32 v127, v127, v232, s19
	v_pk_mul_f32 v[74:75], v[74:75], v[78:79]
	v_pk_mul_f32 v[78:79], v[130:131], v[158:159]
	v_pk_mul_f32 v[76:77], v[76:77], v[80:81]
	v_pk_mul_f32 v[80:81], v[132:133], v[160:161]
	v_pk_mul_f32 v[82:83], v[82:83], v[86:87]
	v_pk_mul_f32 v[86:87], v[134:135], v[166:167]
	v_pk_mul_f32 v[84:85], v[84:85], v[88:89]
	v_pk_mul_f32 v[88:89], v[136:137], v[168:169]
	v_pk_mul_f32 v[90:91], v[90:91], v[94:95]
	v_pk_mul_f32 v[94:95], v[142:143], v[174:175]
	v_pk_mul_f32 v[92:93], v[92:93], v[96:97]
	v_pk_mul_f32 v[96:97], v[144:145], v[176:177]
	v_pk_mul_f32 v[98:99], v[98:99], v[102:103]
	v_pk_mul_f32 v[102:103], v[146:147], v[182:183]
	v_pk_mul_f32 v[100:101], v[100:101], v[104:105]
	v_pk_mul_f32 v[104:105], v[148:149], v[184:185]
	v_pk_mul_f32 v[108:109], v[156:157], v[108:109]
	v_pk_mul_f32 v[106:107], v[154:155], v[106:107]
	v_pk_mul_f32 v[112:113], v[164:165], v[112:113]
	v_pk_mul_f32 v[110:111], v[162:163], v[110:111]
	v_pk_mul_f32 v[114:115], v[114:115], v[118:119]
	v_pk_mul_f32 v[116:117], v[116:117], v[186:187]
	v_pk_mul_f32 v[118:119], v[172:173], v[120:121]
	v_pk_mul_f32 v[120:121], v[170:171], v[188:189]
	v_lshrrev_b32_e32 v34, 16, v34
	v_lshrrev_b32_e32 v67, 16, v179
	v_lshrrev_b32_e32 v68, 16, v128
	v_lshrrev_b32_e32 v69, 16, v126
	v_bfe_u32 v126, v122, 16, 1
	v_bfe_u32 v128, v123, 16, 1
	v_bfe_u32 v130, v70, 16, 1
	v_bfe_u32 v132, v124, 16, 1
	v_bfe_u32 v134, v72, 16, 1
	v_bfe_u32 v131, v71, 16, 1
	v_bfe_u32 v133, v125, 16, 1
	v_bfe_u32 v135, v73, 16, 1
	v_bfe_u32 v136, v78, 16, 1
	v_bfe_u32 v138, v74, 16, 1
	v_bfe_u32 v140, v80, 16, 1
	v_bfe_u32 v142, v76, 16, 1
	v_bfe_u32 v144, v86, 16, 1
	v_bfe_u32 v146, v82, 16, 1
	v_bfe_u32 v148, v88, 16, 1
	v_bfe_u32 v150, v84, 16, 1
	v_bfe_u32 v152, v94, 16, 1
	v_bfe_u32 v154, v90, 16, 1
	v_bfe_u32 v156, v96, 16, 1
	v_bfe_u32 v158, v92, 16, 1
	v_bfe_u32 v160, v102, 16, 1
	v_bfe_u32 v162, v98, 16, 1
	v_bfe_u32 v164, v104, 16, 1
	v_bfe_u32 v166, v100, 16, 1
	v_bfe_u32 v168, v106, 16, 1
	v_bfe_u32 v170, v108, 16, 1
	v_bfe_u32 v172, v110, 16, 1
	v_bfe_u32 v174, v112, 16, 1
	v_bfe_u32 v176, v116, 16, 1
	v_bfe_u32 v179, v114, 16, 1
	v_bfe_u32 v182, v120, 16, 1
	v_bfe_u32 v184, v118, 16, 1
	v_and_or_b32 v190, v178, s18, v34
	v_and_or_b32 v191, v180, s18, v67
	v_and_or_b32 v192, v129, s18, v68
	v_and_or_b32 v193, v127, s18, v69
	v_add3_u32 v34, v122, v126, s19
	v_add3_u32 v122, v123, v128, s19
	v_add3_u32 v70, v70, v130, s19
	v_add3_u32 v123, v124, v132, s19
	v_add3_u32 v72, v72, v134, s19
	v_bfe_u32 v137, v79, 16, 1
	v_bfe_u32 v139, v75, 16, 1
	v_bfe_u32 v141, v81, 16, 1
	v_bfe_u32 v143, v77, 16, 1
	v_bfe_u32 v145, v87, 16, 1
	v_bfe_u32 v147, v83, 16, 1
	v_bfe_u32 v149, v89, 16, 1
	v_bfe_u32 v151, v85, 16, 1
	v_bfe_u32 v153, v95, 16, 1
	v_bfe_u32 v155, v91, 16, 1
	v_bfe_u32 v157, v97, 16, 1
	v_bfe_u32 v159, v93, 16, 1
	v_bfe_u32 v161, v103, 16, 1
	v_bfe_u32 v163, v99, 16, 1
	v_bfe_u32 v165, v105, 16, 1
	v_bfe_u32 v167, v101, 16, 1
	v_bfe_u32 v169, v107, 16, 1
	v_bfe_u32 v171, v109, 16, 1
	v_bfe_u32 v173, v111, 16, 1
	v_bfe_u32 v175, v113, 16, 1
	v_bfe_u32 v177, v117, 16, 1
	v_bfe_u32 v181, v115, 16, 1
	v_bfe_u32 v183, v121, 16, 1
	v_bfe_u32 v185, v119, 16, 1
	v_add3_u32 v71, v71, v131, s19
	v_add3_u32 v124, v125, v133, s19
	v_add3_u32 v73, v73, v135, s19
	v_add3_u32 v78, v78, v136, s19
	v_add3_u32 v74, v74, v138, s19
	v_add3_u32 v80, v80, v140, s19
	v_add3_u32 v76, v76, v142, s19
	v_add3_u32 v86, v86, v144, s19
	v_add3_u32 v82, v82, v146, s19
	v_add3_u32 v88, v88, v148, s19
; __device__ __forceinline__ unsigned pk2(float lo, float hi) { return f2bf(lo) | (f2bf(hi) << 16); }
; __device__ __forceinline__ void ph_conv(Frame& F) {
;     ...
;         for (int tb = 0; tb < 32; tb += 8) {
;             v4u uu[8], bb[8];
; #pragma unroll
;             for (int j = 0; j < 8; ++j) { const size_t off = (size_t)(t0 + tb + j) * D + c; uu[j] = __builtin_nontemporal_load((const v4u*)(U + off)); bb[j] = __builtin_nontemporal_load((const v4u*)(BG + off)); }
;     ...
;                 v4u o; o.x = pk2(yl.x, yl.y); o.y = pk2(yl.z, yl.w); o.z = pk2(yh.x, yh.y); o.w = pk2(yh.z, yh.w);
;                 *(v4u*)(OG + (size_t)(t0 + tb + j) * D + c) = o;
;                 u2l = u1l; u2h = u1h; u1l = u0l; u1h = u0h;
;             }
	v_add3_u32 v84, v84, v150, s19
	v_add3_u32 v94, v94, v152, s19
	v_add3_u32 v90, v90, v154, s19
	v_add3_u32 v96, v96, v156, s19
	v_add3_u32 v92, v92, v158, s19
	v_add3_u32 v102, v102, v160, s19
	v_add3_u32 v98, v98, v162, s19
	v_add3_u32 v104, v104, v164, s19
	v_add3_u32 v100, v100, v166, s19
	v_add3_u32 v106, v106, v168, s19
	v_add3_u32 v108, v108, v170, s19
	v_add3_u32 v110, v110, v172, s19
	v_add3_u32 v112, v112, v174, s19
	v_add3_u32 v116, v116, v176, s19
	v_add3_u32 v114, v114, v179, s19
	v_add3_u32 v120, v120, v182, s19
	v_add3_u32 v118, v118, v184, s19
	v_lshrrev_b32_e32 v34, 16, v34
	v_lshrrev_b32_e32 v62, 16, v70
	v_lshrrev_b32_e32 v63, 16, v123
	v_lshrrev_b32_e32 v69, 16, v72
	v_add3_u32 v79, v79, v137, s19
	v_add3_u32 v75, v75, v139, s19
	v_add3_u32 v81, v81, v141, s19
	v_add3_u32 v77, v77, v143, s19
	v_add3_u32 v87, v87, v145, s19
	v_add3_u32 v83, v83, v147, s19
	v_add3_u32 v89, v89, v149, s19
	v_add3_u32 v85, v85, v151, s19
	v_add3_u32 v95, v95, v153, s19
	v_add3_u32 v91, v91, v155, s19
	v_add3_u32 v97, v97, v157, s19
	v_add3_u32 v93, v93, v159, s19
	v_add3_u32 v103, v103, v161, s19
	v_add3_u32 v99, v99, v163, s19
	v_add3_u32 v105, v105, v165, s19
	v_add3_u32 v101, v101, v167, s19
	v_add3_u32 v107, v107, v169, s19
	v_add3_u32 v109, v109, v171, s19
	v_add3_u32 v111, v111, v173, s19
	v_add3_u32 v113, v113, v175, s19
	v_add3_u32 v117, v117, v177, s19
	v_add3_u32 v115, v115, v181, s19
	v_add3_u32 v121, v121, v183, s19
	v_add3_u32 v119, v119, v185, s19
	v_lshrrev_b32_e32 v70, 16, v78
	v_lshrrev_b32_e32 v72, 16, v74
	v_lshrrev_b32_e32 v74, 16, v80
	v_lshrrev_b32_e32 v76, 16, v76
	v_lshrrev_b32_e32 v78, 16, v86
	v_lshrrev_b32_e32 v80, 16, v82
	v_lshrrev_b32_e32 v82, 16, v88
	v_lshrrev_b32_e32 v84, 16, v84
	v_lshrrev_b32_e32 v86, 16, v94
	v_lshrrev_b32_e32 v88, 16, v90
	v_lshrrev_b32_e32 v90, 16, v96
	v_lshrrev_b32_e32 v92, 16, v92
	v_lshrrev_b32_e32 v94, 16, v102
	v_lshrrev_b32_e32 v96, 16, v98
	v_lshrrev_b32_e32 v98, 16, v104
	v_lshrrev_b32_e32 v100, 16, v100
	v_lshrrev_b32_e32 v102, 16, v106
	v_lshrrev_b32_e32 v104, 16, v108
	v_lshrrev_b32_e32 v106, 16, v110
	v_lshrrev_b32_e32 v108, 16, v112
	v_lshrrev_b32_e32 v110, 16, v116
	v_lshrrev_b32_e32 v112, 16, v114
	v_lshrrev_b32_e32 v114, 16, v120
	v_lshrrev_b32_e32 v116, 16, v118
	v_and_or_b32 v194, v122, s18, v34
	v_and_or_b32 v195, v71, s18, v62
	v_and_or_b32 v196, v124, s18, v63
	v_and_or_b32 v197, v73, s18, v69
	v_and_or_b32 v198, v79, s18, v70
	v_and_or_b32 v199, v75, s18, v72
	v_and_or_b32 v200, v81, s18, v74
	v_and_or_b32 v201, v77, s18, v76
	v_and_or_b32 v202, v87, s18, v78
	v_and_or_b32 v203, v83, s18, v80
	v_and_or_b32 v204, v89, s18, v82
	v_and_or_b32 v205, v85, s18, v84
	v_and_or_b32 v206, v95, s18, v86
	v_and_or_b32 v207, v91, s18, v88
	v_and_or_b32 v208, v97, s18, v90
	v_and_or_b32 v209, v93, s18, v92
	v_and_or_b32 v210, v103, s18, v94
	v_and_or_b32 v211, v99, s18, v96
	v_and_or_b32 v212, v105, s18, v98
	v_and_or_b32 v213, v101, s18, v100
	v_and_or_b32 v214, v107, s18, v102
	v_and_or_b32 v215, v109, s18, v104
	v_and_or_b32 v216, v111, s18, v106
	v_and_or_b32 v217, v113, s18, v108
	v_and_or_b32 v218, v117, s18, v110
	v_and_or_b32 v219, v115, s18, v112
	v_and_or_b32 v220, v121, s18, v114
	v_and_or_b32 v221, v119, s18, v116
	v_mov_b32_e32 v246, v48
	v_mov_b32_e32 v247, v49
	v_mov_b32_e32 v248, v52
	v_mov_b32_e32 v249, v53
	v_mov_b32_e32 v250, v56
	v_mov_b32_e32 v251, v57
	v_mov_b32_e32 v252, v60
	v_mov_b32_e32 v253, v61
.Lmy_cv_loop:
	v_add_u32_e32 v34, s16, v64
	v_add_u32_e32 v56, 8, v34
	v_add_u32_e32 v58, 9, v34
	v_add_u32_e32 v60, 10, v34
	v_add_u32_e32 v62, 11, v34
	v_add_u32_e32 v66, 12, v34
	v_add_u32_e32 v68, 13, v34
	v_add_u32_e32 v70, 14, v34
	v_add_u32_e32 v72, 15, v34
	v_pk_mul_f32 v[48:49], v[12:13], v[28:29]
	v_pk_mul_f32 v[50:51], v[10:11], v[26:27]
	v_pk_mul_f32 v[52:53], v[20:21], v[32:33]
	v_pk_mul_f32 v[54:55], v[18:19], v[30:31]
	v_ashrrev_i32_e32 v57, 31, v56
	v_ashrrev_i32_e32 v59, 31, v58
	v_ashrrev_i32_e32 v61, 31, v60
	v_ashrrev_i32_e32 v63, 31, v62
	v_ashrrev_i32_e32 v67, 31, v66
	v_ashrrev_i32_e32 v69, 31, v68
	v_ashrrev_i32_e32 v71, 31, v70
	v_ashrrev_i32_e32 v73, 31, v72
	v_pk_fma_f32 v[122:123], v[8:9], v[42:43], v[48:49]
	v_pk_fma_f32 v[124:125], v[6:7], v[40:41], v[50:51]
	v_pk_fma_f32 v[126:127], v[4:5], v[46:47], v[52:53]
	v_pk_fma_f32 v[128:129], v[2:3], v[44:45], v[54:55]
	v_lshlrev_b64 v[40:41], 12, v[56:57]
	v_lshlrev_b64 v[42:43], 12, v[58:59]
	v_lshlrev_b64 v[44:45], 12, v[60:61]
	v_lshlrev_b64 v[46:47], 12, v[62:63]
	v_lshlrev_b64 v[54:55], 12, v[66:67]
	v_lshlrev_b64 v[56:57], 12, v[68:69]
	v_lshlrev_b64 v[58:59], 12, v[70:71]
	v_lshlrev_b64 v[60:61], 12, v[72:73]
	v_or_b32_e32 v66, v40, v65
	v_mov_b32_e32 v67, v41
	v_or_b32_e32 v68, v42, v65
	v_mov_b32_e32 v69, v43
	v_or_b32_e32 v70, v44, v65
	v_mov_b32_e32 v71, v45
	v_or_b32_e32 v72, v46, v65
	v_mov_b32_e32 v73, v47
	v_or_b32_e32 v74, v54, v65
	v_mov_b32_e32 v75, v55
	v_or_b32_e32 v76, v56, v65
	v_mov_b32_e32 v77, v57
	v_or_b32_e32 v78, v58, v65
	v_mov_b32_e32 v79, v59
	v_or_b32_e32 v80, v60, v65
	v_mov_b32_e32 v81, v61
	v_lshl_add_u64 v[86:87], s[14:15], 0, v[66:67]
	v_lshl_add_u64 v[88:89], s[10:11], 0, v[66:67]
	v_lshl_add_u64 v[90:91], s[14:15], 0, v[68:69]
	v_lshl_add_u64 v[92:93], s[10:11], 0, v[68:69]
	v_lshl_add_u64 v[94:95], s[14:15], 0, v[70:71]
	v_lshl_add_u64 v[96:97], s[10:11], 0, v[70:71]
	v_lshl_add_u64 v[98:99], s[14:15], 0, v[72:73]
	v_lshl_add_u64 v[102:103], s[10:11], 0, v[72:73]
	v_lshl_add_u64 v[104:105], s[14:15], 0, v[74:75]
	v_lshl_add_u64 v[106:107], s[10:11], 0, v[74:75]
	v_lshl_add_u64 v[108:109], s[14:15], 0, v[76:77]
	v_lshl_add_u64 v[110:111], s[10:11], 0, v[76:77]
; __device__ __forceinline__ unsigned pk2(float lo, float hi) { return f2bf(lo) | (f2bf(hi) << 16); }
; __device__ __forceinline__ f32x4 bf4lo(const v4u& w) { return (f32x4){bflo(w.x), bfhi(w.x), bflo(w.y), bfhi(w.y)}; }
; __device__ __forceinline__ f32x4 bf4hi(const v4u& w) { return (f32x4){bflo(w.z), bfhi(w.z), bflo(w.w), bfhi(w.w)}; }
; __device__ __forceinline__ void ph_conv(Frame& F) {
;     ...
;         for (int tb = 0; tb < 32; tb += 8) {
;             v4u uu[8], bb[8];
; #pragma unroll
;             for (int j = 0; j < 8; ++j) { const size_t off = (size_t)(t0 + tb + j) * D + c; uu[j] = __builtin_nontemporal_load((const v4u*)(U + off)); bb[j] = __builtin_nontemporal_load((const v4u*)(BG + off)); }
; #pragma unroll
;             for (int j = 0; j < 8; ++j) {
;                 const f32x4 u0l = bf4lo(uu[j]), u0h = bf4hi(uu[j]), bl = bf4lo(bb[j]), bh = bf4hi(bb[j]);
;                 const f32x4 yl = bl * (wa0 * u2l + wb0 * u1l + wc0 * u0l), yh = bh * (wa1 * u2h + wb1 * u1h + wc1 * u0h);
;                 v4u o; o.x = pk2(yl.x, yl.y); o.y = pk2(yl.z, yl.w); o.z = pk2(yh.x, yh.y); o.w = pk2(yh.z, yh.w);
;                 *(v4u*)(OG + (size_t)(t0 + tb + j) * D + c) = o;
	v_lshl_add_u64 v[112:113], s[14:15], 0, v[78:79]
	v_lshl_add_u64 v[114:115], s[10:11], 0, v[78:79]
	v_lshl_add_u64 v[116:117], s[14:15], 0, v[80:81]
	v_lshl_add_u64 v[118:119], s[10:11], 0, v[80:81]
	v_lshl_add_u64 v[62:63], v[38:39], 0, v[40:41]
	v_lshl_add_u64 v[48:49], v[38:39], 0, v[42:43]
	v_lshl_add_u64 v[50:51], v[38:39], 0, v[44:45]
	v_lshl_add_u64 v[52:53], v[38:39], 0, v[46:47]
	global_load_dwordx4 v[40:43], v[86:87], off nt
	global_load_dwordx4 v[44:47], v[88:89], off nt
	global_load_dwordx4 v[66:69], v[90:91], off nt
	global_load_dwordx4 v[70:73], v[92:93], off nt
	global_load_dwordx4 v[74:77], v[94:95], off nt
	global_load_dwordx4 v[78:81], v[96:97], off nt
	global_load_dwordx4 v[82:85], v[98:99], off nt
	global_load_dwordx4 v[86:89], v[102:103], off nt
	s_nop 0
	global_load_dwordx4 v[90:93], v[104:105], off nt
	global_load_dwordx4 v[94:97], v[106:107], off nt
	global_load_dwordx4 v[98:101], v[108:109], off nt
	s_nop 0
	global_load_dwordx4 v[102:105], v[110:111], off nt
	global_load_dwordx4 v[106:109], v[112:113], off nt
	s_nop 0
	global_load_dwordx4 v[110:113], v[114:115], off nt
	s_nop 0
	global_load_dwordx4 v[114:117], v[116:117], off nt
	s_nop 0
	global_load_dwordx4 v[118:121], v[118:119], off nt
	global_store_dwordx4 v[246:247], v[190:193], off offset:-4096
	global_store_dwordx4 v[246:247], v[194:197], off
	global_store_dwordx4 v[248:249], v[198:201], off offset:-4096
	global_store_dwordx4 v[248:249], v[202:205], off
	global_store_dwordx4 v[250:251], v[206:209], off offset:-4096
	global_store_dwordx4 v[250:251], v[210:213], off
	global_store_dwordx4 v[252:253], v[214:217], off offset:-4096
	global_store_dwordx4 v[252:253], v[218:221], off
	s_add_i32 s16, s16, 8
	s_cmp_gt_u32 s16, 23
	v_lshl_add_u64 v[54:55], v[38:39], 0, v[54:55]
	v_lshl_add_u64 v[56:57], v[38:39], 0, v[56:57]
	v_lshl_add_u64 v[58:59], v[38:39], 0, v[58:59]
	v_lshl_add_u64 v[60:61], v[38:39], 0, v[60:61]
	s_waitcnt vmcnt(23)
	v_lshlrev_b32_e32 v130, 16, v40
	v_and_b32_e32 v131, 0xffff0000, v40
	v_lshlrev_b32_e32 v132, 16, v41
	v_and_b32_e32 v133, 0xffff0000, v41
	v_lshlrev_b32_e32 v134, 16, v42
	v_and_b32_e32 v135, 0xffff0000, v42
	v_lshlrev_b32_e32 v136, 16, v43
	v_and_b32_e32 v137, 0xffff0000, v43
	s_waitcnt vmcnt(22)
	v_lshlrev_b32_e32 v138, 16, v44
	v_and_b32_e32 v139, 0xffff0000, v44
	v_lshlrev_b32_e32 v140, 16, v45
	v_and_b32_e32 v141, 0xffff0000, v45
	v_lshlrev_b32_e32 v142, 16, v46
	v_and_b32_e32 v143, 0xffff0000, v46
	v_lshlrev_b32_e32 v144, 16, v47
	v_and_b32_e32 v145, 0xffff0000, v47
	s_waitcnt vmcnt(21)
	v_lshlrev_b32_e32 v146, 16, v66
	v_and_b32_e32 v147, 0xffff0000, v66
	v_lshlrev_b32_e32 v66, 16, v67
	v_and_b32_e32 v67, 0xffff0000, v67
	v_lshlrev_b32_e32 v148, 16, v68
	v_and_b32_e32 v149, 0xffff0000, v68
	v_lshlrev_b32_e32 v68, 16, v69
	v_and_b32_e32 v69, 0xffff0000, v69
	s_waitcnt vmcnt(19)
	v_lshlrev_b32_e32 v154, 16, v74
	v_and_b32_e32 v155, 0xffff0000, v74
	v_lshlrev_b32_e32 v74, 16, v75
	v_and_b32_e32 v75, 0xffff0000, v75
	v_lshlrev_b32_e32 v156, 16, v76
	v_and_b32_e32 v157, 0xffff0000, v76
	v_lshlrev_b32_e32 v76, 16, v77
	v_and_b32_e32 v77, 0xffff0000, v77
	s_waitcnt vmcnt(17)
	v_lshlrev_b32_e32 v162, 16, v82
	v_and_b32_e32 v163, 0xffff0000, v82
	v_lshlrev_b32_e32 v82, 16, v83
	v_and_b32_e32 v83, 0xffff0000, v83
	v_lshlrev_b32_e32 v164, 16, v84
	v_and_b32_e32 v165, 0xffff0000, v84
	v_lshlrev_b32_e32 v84, 16, v85
	v_and_b32_e32 v85, 0xffff0000, v85
	s_waitcnt vmcnt(15)
	v_lshlrev_b32_e32 v170, 16, v90
	v_and_b32_e32 v171, 0xffff0000, v90
	v_lshlrev_b32_e32 v90, 16, v91
	v_and_b32_e32 v91, 0xffff0000, v91
	v_lshlrev_b32_e32 v172, 16, v92
	v_and_b32_e32 v173, 0xffff0000, v92
	v_lshlrev_b32_e32 v92, 16, v93
	v_and_b32_e32 v93, 0xffff0000, v93
	s_waitcnt vmcnt(13)
	v_lshlrev_b32_e32 v178, 16, v98
	v_and_b32_e32 v179, 0xffff0000, v98
	v_lshlrev_b32_e32 v98, 16, v99
	v_and_b32_e32 v99, 0xffff0000, v99
	v_lshlrev_b32_e32 v180, 16, v100
	v_and_b32_e32 v181, 0xffff0000, v100
	v_lshlrev_b32_e32 v100, 16, v101
	v_and_b32_e32 v101, 0xffff0000, v101
	s_waitcnt vmcnt(11)
	v_lshlrev_b32_e32 v40, 16, v106
	v_and_b32_e32 v41, 0xffff0000, v106
	v_lshlrev_b32_e32 v42, 16, v107
	v_and_b32_e32 v43, 0xffff0000, v107
	v_lshlrev_b32_e32 v44, 16, v108
	v_and_b32_e32 v45, 0xffff0000, v108
	v_lshlrev_b32_e32 v46, 16, v109
	v_and_b32_e32 v47, 0xffff0000, v109
	v_pk_fma_f32 v[124:125], v[14:15], v[130:131], v[124:125]
	v_pk_fma_f32 v[122:123], v[16:17], v[132:133], v[122:123]
	v_pk_fma_f32 v[128:129], v[22:23], v[134:135], v[128:129]
	v_pk_fma_f32 v[126:127], v[24:25], v[136:137], v[126:127]
	v_pk_mul_f32 v[190:191], v[10:11], v[130:131]
	v_pk_mul_f32 v[192:193], v[12:13], v[132:133]
	v_pk_mul_f32 v[194:195], v[18:19], v[134:135]
	v_pk_mul_f32 v[196:197], v[20:21], v[136:137]
	v_pk_mul_f32 v[198:199], v[10:11], v[146:147]
	v_pk_mul_f32 v[200:201], v[12:13], v[66:67]
	v_pk_mul_f32 v[202:203], v[18:19], v[148:149]
	v_pk_mul_f32 v[204:205], v[20:21], v[68:69]
	v_pk_mul_f32 v[206:207], v[10:11], v[154:155]
	v_pk_mul_f32 v[208:209], v[12:13], v[74:75]
	v_pk_mul_f32 v[210:211], v[18:19], v[156:157]
	v_pk_mul_f32 v[212:213], v[20:21], v[76:77]
	v_pk_mul_f32 v[214:215], v[10:11], v[162:163]
	v_pk_mul_f32 v[216:217], v[12:13], v[82:83]
	v_pk_mul_f32 v[218:219], v[18:19], v[164:165]
	v_pk_mul_f32 v[220:221], v[20:21], v[84:85]
	v_pk_mul_f32 v[222:223], v[10:11], v[170:171]
	v_pk_mul_f32 v[224:225], v[12:13], v[90:91]
	v_pk_mul_f32 v[226:227], v[18:19], v[172:173]
	v_pk_mul_f32 v[228:229], v[20:21], v[92:93]
	v_pk_mul_f32 v[230:231], v[10:11], v[178:179]
	v_pk_mul_f32 v[232:233], v[12:13], v[98:99]
	v_pk_mul_f32 v[234:235], v[18:19], v[180:181]
	v_pk_mul_f32 v[236:237], v[20:21], v[100:101]
; __device__ __forceinline__ f32x4 bf4lo(const v4u& w) { return (f32x4){bflo(w.x), bfhi(w.x), bflo(w.y), bfhi(w.y)}; }
; __device__ __forceinline__ f32x4 bf4hi(const v4u& w) { return (f32x4){bflo(w.z), bfhi(w.z), bflo(w.w), bfhi(w.w)}; }
; __device__ __forceinline__ void ph_conv(Frame& F) {
;     ...
;             for (int j = 0; j < 8; ++j) {
;                 const f32x4 u0l = bf4lo(uu[j]), u0h = bf4hi(uu[j]), bl = bf4lo(bb[j]), bh = bf4hi(bb[j]);
;                 const f32x4 yl = bl * (wa0 * u2l + wb0 * u1l + wc0 * u0l), yh = bh * (wa1 * u2h + wb1 * u1h + wc1 * u0h);
	v_pk_mul_f32 v[238:239], v[10:11], v[40:41]
	v_pk_mul_f32 v[240:241], v[12:13], v[42:43]
	v_pk_mul_f32 v[242:243], v[18:19], v[44:45]
	v_pk_mul_f32 v[244:245], v[20:21], v[46:47]
	v_pk_mul_f32 v[122:123], v[122:123], v[140:141]
	v_pk_mul_f32 v[124:125], v[124:125], v[138:139]
	v_pk_mul_f32 v[126:127], v[126:127], v[144:145]
	v_pk_mul_f32 v[128:129], v[128:129], v[142:143]
	v_pk_fma_f32 v[138:139], v[8:9], v[28:29], v[192:193]
	v_pk_fma_f32 v[140:141], v[6:7], v[26:27], v[190:191]
	v_pk_fma_f32 v[142:143], v[4:5], v[32:33], v[196:197]
	v_pk_fma_f32 v[144:145], v[2:3], v[30:31], v[194:195]
	v_lshlrev_b32_e32 v150, 16, v70
	v_and_b32_e32 v151, 0xffff0000, v70
	v_lshlrev_b32_e32 v70, 16, v71
	v_and_b32_e32 v71, 0xffff0000, v71
	v_lshlrev_b32_e32 v152, 16, v72
	v_and_b32_e32 v153, 0xffff0000, v72
	v_lshlrev_b32_e32 v72, 16, v73
	v_and_b32_e32 v73, 0xffff0000, v73
	v_pk_fma_f32 v[132:133], v[8:9], v[132:133], v[200:201]
	v_pk_fma_f32 v[130:131], v[6:7], v[130:131], v[198:199]
	v_pk_fma_f32 v[136:137], v[4:5], v[136:137], v[204:205]
	v_pk_fma_f32 v[134:135], v[2:3], v[134:135], v[202:203]
	v_pk_fma_f32 v[190:191], v[8:9], v[66:67], v[208:209]
	v_pk_fma_f32 v[192:193], v[6:7], v[146:147], v[206:207]
	v_pk_fma_f32 v[194:195], v[4:5], v[68:69], v[212:213]
	v_pk_fma_f32 v[196:197], v[2:3], v[148:149], v[210:211]
	v_pk_fma_f32 v[198:199], v[8:9], v[74:75], v[216:217]
	v_pk_fma_f32 v[200:201], v[6:7], v[154:155], v[214:215]
	v_pk_fma_f32 v[202:203], v[4:5], v[76:77], v[220:221]
	v_pk_fma_f32 v[204:205], v[2:3], v[156:157], v[218:219]
	v_pk_fma_f32 v[206:207], v[8:9], v[82:83], v[224:225]
	v_pk_fma_f32 v[208:209], v[6:7], v[162:163], v[222:223]
	v_pk_fma_f32 v[210:211], v[4:5], v[84:85], v[228:229]
	v_pk_fma_f32 v[212:213], v[2:3], v[164:165], v[226:227]
	v_pk_fma_f32 v[214:215], v[8:9], v[90:91], v[232:233]
	v_pk_fma_f32 v[216:217], v[6:7], v[170:171], v[230:231]
	v_pk_fma_f32 v[218:219], v[4:5], v[92:93], v[236:237]
	v_pk_fma_f32 v[220:221], v[2:3], v[172:173], v[234:235]
	s_waitcnt vmcnt(9)
	v_lshlrev_b32_e32 v26, 16, v114
	v_and_b32_e32 v27, 0xffff0000, v114
	v_lshlrev_b32_e32 v28, 16, v115
	v_and_b32_e32 v29, 0xffff0000, v115
	v_lshlrev_b32_e32 v30, 16, v116
	v_and_b32_e32 v31, 0xffff0000, v116
	v_lshlrev_b32_e32 v32, 16, v117
	v_and_b32_e32 v33, 0xffff0000, v117
	v_pk_fma_f32 v[114:115], v[8:9], v[98:99], v[240:241]
	v_pk_fma_f32 v[116:117], v[6:7], v[178:179], v[238:239]
	v_pk_fma_f32 v[222:223], v[4:5], v[100:101], v[244:245]
	v_pk_fma_f32 v[224:225], v[2:3], v[180:181], v[242:243]
	v_bfe_u32 v34, v124, 16, 1
	v_bfe_u32 v226, v125, 16, 1
	v_bfe_u32 v227, v122, 16, 1
	v_bfe_u32 v228, v123, 16, 1
	v_bfe_u32 v229, v128, 16, 1
	v_bfe_u32 v231, v126, 16, 1
	v_pk_fma_f32 v[140:141], v[14:15], v[146:147], v[140:141]
	v_pk_fma_f32 v[66:67], v[16:17], v[66:67], v[138:139]
	v_pk_fma_f32 v[138:139], v[22:23], v[148:149], v[144:145]
	v_pk_fma_f32 v[68:69], v[24:25], v[68:69], v[142:143]
	v_lshlrev_b32_e32 v158, 16, v78
	v_and_b32_e32 v159, 0xffff0000, v78
	v_lshlrev_b32_e32 v78, 16, v79
	v_and_b32_e32 v79, 0xffff0000, v79
	v_lshlrev_b32_e32 v160, 16, v80
	v_and_b32_e32 v161, 0xffff0000, v80
	v_lshlrev_b32_e32 v80, 16, v81
	v_and_b32_e32 v81, 0xffff0000, v81
	v_lshlrev_b32_e32 v166, 16, v86
	v_and_b32_e32 v167, 0xffff0000, v86
	v_lshlrev_b32_e32 v86, 16, v87
	v_and_b32_e32 v87, 0xffff0000, v87
	v_lshlrev_b32_e32 v168, 16, v88
	v_and_b32_e32 v169, 0xffff0000, v88
	v_lshlrev_b32_e32 v88, 16, v89
	v_and_b32_e32 v89, 0xffff0000, v89
	v_lshlrev_b32_e32 v174, 16, v94
	v_and_b32_e32 v175, 0xffff0000, v94
	v_lshlrev_b32_e32 v94, 16, v95
	v_and_b32_e32 v95, 0xffff0000, v95
	v_lshlrev_b32_e32 v176, 16, v96
	v_and_b32_e32 v177, 0xffff0000, v96
	v_lshlrev_b32_e32 v96, 16, v97
	v_and_b32_e32 v97, 0xffff0000, v97
	v_lshlrev_b32_e32 v182, 16, v102
	v_and_b32_e32 v183, 0xffff0000, v102
	v_lshlrev_b32_e32 v102, 16, v103
	v_and_b32_e32 v103, 0xffff0000, v103
	v_lshlrev_b32_e32 v184, 16, v104
	v_and_b32_e32 v185, 0xffff0000, v104
	v_lshlrev_b32_e32 v104, 16, v105
	v_and_b32_e32 v105, 0xffff0000, v105
	v_lshlrev_b32_e32 v106, 16, v110
	v_and_b32_e32 v107, 0xffff0000, v110
	v_lshlrev_b32_e32 v108, 16, v111
	v_and_b32_e32 v109, 0xffff0000, v111
	v_lshlrev_b32_e32 v110, 16, v112
	v_and_b32_e32 v111, 0xffff0000, v112
	v_lshlrev_b32_e32 v112, 16, v113
	v_and_b32_e32 v113, 0xffff0000, v113
	s_waitcnt vmcnt(8)
; __device__ __forceinline__ unsigned f2bf(float f) { unsigned u = __builtin_bit_cast(unsigned, f); return (u + 0x7fffu + ((u >> 16) & 1u)) >> 16; }
; __device__ __forceinline__ unsigned pk2(float lo, float hi) { return f2bf(lo) | (f2bf(hi) << 16); }
; __device__ __forceinline__ void ph_conv(Frame& F) {
;     ...
;                 const f32x4 yl = bl * (wa0 * u2l + wb0 * u1l + wc0 * u0l), yh = bh * (wa1 * u2h + wb1 * u1h + wc1 * u0h);
;                 v4u o; o.x = pk2(yl.x, yl.y); o.y = pk2(yl.z, yl.w); o.z = pk2(yh.x, yh.y); o.w = pk2(yh.z, yh.w);
	v_lshlrev_b32_e32 v186, 16, v118
	v_and_b32_e32 v187, 0xffff0000, v118
	v_lshlrev_b32_e32 v118, 16, v119
	v_and_b32_e32 v119, 0xffff0000, v119
	v_lshlrev_b32_e32 v188, 16, v120
	v_and_b32_e32 v189, 0xffff0000, v120
	v_lshlrev_b32_e32 v120, 16, v121
	v_and_b32_e32 v121, 0xffff0000, v121
	v_bfe_u32 v230, v129, 16, 1
	v_bfe_u32 v232, v127, 16, 1
	v_pk_fma_f32 v[130:131], v[14:15], v[154:155], v[130:131]
	v_pk_fma_f32 v[74:75], v[16:17], v[74:75], v[132:133]
	v_pk_fma_f32 v[132:133], v[22:23], v[156:157], v[134:135]
	v_pk_fma_f32 v[76:77], v[24:25], v[76:77], v[136:137]
	v_pk_fma_f32 v[134:135], v[14:15], v[162:163], v[192:193]
	v_pk_fma_f32 v[82:83], v[16:17], v[82:83], v[190:191]
	v_pk_fma_f32 v[136:137], v[22:23], v[164:165], v[196:197]
	v_pk_fma_f32 v[84:85], v[24:25], v[84:85], v[194:195]
	v_pk_fma_f32 v[142:143], v[14:15], v[170:171], v[200:201]
	v_pk_fma_f32 v[90:91], v[16:17], v[90:91], v[198:199]
	v_pk_fma_f32 v[144:145], v[22:23], v[172:173], v[204:205]
	v_pk_fma_f32 v[92:93], v[24:25], v[92:93], v[202:203]
	v_pk_fma_f32 v[146:147], v[14:15], v[178:179], v[208:209]
	v_pk_fma_f32 v[98:99], v[16:17], v[98:99], v[206:207]
	v_pk_fma_f32 v[148:149], v[22:23], v[180:181], v[212:213]
	v_pk_fma_f32 v[100:101], v[24:25], v[100:101], v[210:211]
	v_pk_fma_f32 v[154:155], v[14:15], v[40:41], v[216:217]
	v_pk_fma_f32 v[156:157], v[16:17], v[42:43], v[214:215]
	v_pk_fma_f32 v[162:163], v[22:23], v[44:45], v[220:221]
	v_pk_fma_f32 v[164:165], v[24:25], v[46:47], v[218:219]
	v_pk_fma_f32 v[116:117], v[14:15], v[26:27], v[116:117]
	v_pk_fma_f32 v[114:115], v[16:17], v[28:29], v[114:115]
	v_pk_fma_f32 v[170:171], v[22:23], v[30:31], v[224:225]
	v_pk_fma_f32 v[172:173], v[24:25], v[32:33], v[222:223]
	v_add3_u32 v34, v124, v34, s19
	v_add3_u32 v178, v125, v226, s19
	v_add3_u32 v179, v122, v227, s19
	v_add3_u32 v180, v123, v228, s19
	v_add3_u32 v128, v128, v229, s19
	v_add3_u32 v126, v126, v231, s19
	v_pk_mul_f32 v[70:71], v[66:67], v[70:71]
	v_pk_mul_f32 v[122:123], v[140:141], v[150:151]
	v_pk_mul_f32 v[72:73], v[68:69], v[72:73]
	v_pk_mul_f32 v[124:125], v[138:139], v[152:153]
	v_add3_u32 v129, v129, v230, s19
	v_add3_u32 v127, v127, v232, s19
	v_pk_mul_f32 v[74:75], v[74:75], v[78:79]
	v_pk_mul_f32 v[78:79], v[130:131], v[158:159]
	v_pk_mul_f32 v[76:77], v[76:77], v[80:81]
	v_pk_mul_f32 v[80:81], v[132:133], v[160:161]
	v_pk_mul_f32 v[82:83], v[82:83], v[86:87]
	v_pk_mul_f32 v[86:87], v[134:135], v[166:167]
	v_pk_mul_f32 v[84:85], v[84:85], v[88:89]
	v_pk_mul_f32 v[88:89], v[136:137], v[168:169]
	v_pk_mul_f32 v[90:91], v[90:91], v[94:95]
	v_pk_mul_f32 v[94:95], v[142:143], v[174:175]
	v_pk_mul_f32 v[92:93], v[92:93], v[96:97]
	v_pk_mul_f32 v[96:97], v[144:145], v[176:177]
	v_pk_mul_f32 v[98:99], v[98:99], v[102:103]
	v_pk_mul_f32 v[102:103], v[146:147], v[182:183]
	v_pk_mul_f32 v[100:101], v[100:101], v[104:105]
	v_pk_mul_f32 v[104:105], v[148:149], v[184:185]
	v_pk_mul_f32 v[108:109], v[156:157], v[108:109]
	v_pk_mul_f32 v[106:107], v[154:155], v[106:107]
	v_pk_mul_f32 v[112:113], v[164:165], v[112:113]
	v_pk_mul_f32 v[110:111], v[162:163], v[110:111]
	v_pk_mul_f32 v[114:115], v[114:115], v[118:119]
	v_pk_mul_f32 v[116:117], v[116:117], v[186:187]
	v_pk_mul_f32 v[118:119], v[172:173], v[120:121]
	v_pk_mul_f32 v[120:121], v[170:171], v[188:189]
	v_lshrrev_b32_e32 v34, 16, v34
	v_lshrrev_b32_e32 v67, 16, v179
	v_lshrrev_b32_e32 v68, 16, v128
	v_lshrrev_b32_e32 v69, 16, v126
	v_bfe_u32 v126, v122, 16, 1
	v_bfe_u32 v128, v123, 16, 1
	v_bfe_u32 v130, v70, 16, 1
	v_bfe_u32 v132, v124, 16, 1
	v_bfe_u32 v134, v72, 16, 1
	v_bfe_u32 v131, v71, 16, 1
	v_bfe_u32 v133, v125, 16, 1
	v_bfe_u32 v135, v73, 16, 1
	v_bfe_u32 v136, v78, 16, 1
	v_bfe_u32 v138, v74, 16, 1
	v_bfe_u32 v140, v80, 16, 1
	v_bfe_u32 v142, v76, 16, 1
	v_bfe_u32 v144, v86, 16, 1
	v_bfe_u32 v146, v82, 16, 1
	v_bfe_u32 v148, v88, 16, 1
	v_bfe_u32 v150, v84, 16, 1
	v_bfe_u32 v152, v94, 16, 1
	v_bfe_u32 v154, v90, 16, 1
	v_bfe_u32 v156, v96, 16, 1
	v_bfe_u32 v158, v92, 16, 1
	v_bfe_u32 v160, v102, 16, 1
	v_bfe_u32 v162, v98, 16, 1
	v_bfe_u32 v164, v104, 16, 1
	v_bfe_u32 v166, v100, 16, 1
	v_bfe_u32 v168, v106, 16, 1
	v_bfe_u32 v170, v108, 16, 1
	v_bfe_u32 v172, v110, 16, 1
	v_bfe_u32 v174, v112, 16, 1
	v_bfe_u32 v176, v116, 16, 1
	v_bfe_u32 v179, v114, 16, 1
	v_bfe_u32 v182, v120, 16, 1
	v_bfe_u32 v184, v118, 16, 1
	v_and_or_b32 v190, v178, s18, v34
	v_and_or_b32 v191, v180, s18, v67
	v_and_or_b32 v192, v129, s18, v68
	v_and_or_b32 v193, v127, s18, v69
	v_add3_u32 v34, v122, v126, s19
	v_add3_u32 v122, v123, v128, s19
	v_add3_u32 v70, v70, v130, s19
	v_add3_u32 v123, v124, v132, s19
	v_add3_u32 v72, v72, v134, s19
	v_bfe_u32 v137, v79, 16, 1
	v_bfe_u32 v139, v75, 16, 1
	v_bfe_u32 v141, v81, 16, 1
	v_bfe_u32 v143, v77, 16, 1
	v_bfe_u32 v145, v87, 16, 1
	v_bfe_u32 v147, v83, 16, 1
	v_bfe_u32 v149, v89, 16, 1
; __device__ __forceinline__ unsigned pk2(float lo, float hi) { return f2bf(lo) | (f2bf(hi) << 16); }
; __device__ __forceinline__ void ph_conv(Frame& F) {
;     ...
;                 v4u o; o.x = pk2(yl.x, yl.y); o.y = pk2(yl.z, yl.w); o.z = pk2(yh.x, yh.y); o.w = pk2(yh.z, yh.w);
;                 *(v4u*)(OG + (size_t)(t0 + tb + j) * D + c) = o;
;                 u2l = u1l; u2h = u1h; u1l = u0l; u1h = u0h;
;             }
;         }
;     }
	v_bfe_u32 v151, v85, 16, 1
	v_bfe_u32 v153, v95, 16, 1
	v_bfe_u32 v155, v91, 16, 1
	v_bfe_u32 v157, v97, 16, 1
	v_bfe_u32 v159, v93, 16, 1
	v_bfe_u32 v161, v103, 16, 1
	v_bfe_u32 v163, v99, 16, 1
	v_bfe_u32 v165, v105, 16, 1
	v_bfe_u32 v167, v101, 16, 1
	v_bfe_u32 v169, v107, 16, 1
	v_bfe_u32 v171, v109, 16, 1
	v_bfe_u32 v173, v111, 16, 1
	v_bfe_u32 v175, v113, 16, 1
	v_bfe_u32 v177, v117, 16, 1
	v_bfe_u32 v181, v115, 16, 1
	v_bfe_u32 v183, v121, 16, 1
	v_bfe_u32 v185, v119, 16, 1
	v_add3_u32 v71, v71, v131, s19
	v_add3_u32 v124, v125, v133, s19
	v_add3_u32 v73, v73, v135, s19
	v_add3_u32 v78, v78, v136, s19
	v_add3_u32 v74, v74, v138, s19
	v_add3_u32 v80, v80, v140, s19
	v_add3_u32 v76, v76, v142, s19
	v_add3_u32 v86, v86, v144, s19
	v_add3_u32 v82, v82, v146, s19
	v_add3_u32 v88, v88, v148, s19
	v_add3_u32 v84, v84, v150, s19
	v_add3_u32 v94, v94, v152, s19
	v_add3_u32 v90, v90, v154, s19
	v_add3_u32 v96, v96, v156, s19
	v_add3_u32 v92, v92, v158, s19
	v_add3_u32 v102, v102, v160, s19
	v_add3_u32 v98, v98, v162, s19
	v_add3_u32 v104, v104, v164, s19
	v_add3_u32 v100, v100, v166, s19
	v_add3_u32 v106, v106, v168, s19
	v_add3_u32 v108, v108, v170, s19
	v_add3_u32 v110, v110, v172, s19
	v_add3_u32 v112, v112, v174, s19
	v_add3_u32 v116, v116, v176, s19
	v_add3_u32 v114, v114, v179, s19
	v_add3_u32 v120, v120, v182, s19
	v_add3_u32 v118, v118, v184, s19
	v_lshrrev_b32_e32 v34, 16, v34
	v_lshrrev_b32_e32 v62, 16, v70
	v_lshrrev_b32_e32 v63, 16, v123
	v_lshrrev_b32_e32 v69, 16, v72
	v_add3_u32 v79, v79, v137, s19
	v_add3_u32 v75, v75, v139, s19
	v_add3_u32 v81, v81, v141, s19
	v_add3_u32 v77, v77, v143, s19
	v_add3_u32 v87, v87, v145, s19
	v_add3_u32 v83, v83, v147, s19
	v_add3_u32 v89, v89, v149, s19
	v_add3_u32 v85, v85, v151, s19
	v_add3_u32 v95, v95, v153, s19
	v_add3_u32 v91, v91, v155, s19
	v_add3_u32 v97, v97, v157, s19
	v_add3_u32 v93, v93, v159, s19
	v_add3_u32 v103, v103, v161, s19
	v_add3_u32 v99, v99, v163, s19
	v_add3_u32 v105, v105, v165, s19
	v_add3_u32 v101, v101, v167, s19
	v_add3_u32 v107, v107, v169, s19
	v_add3_u32 v109, v109, v171, s19
	v_add3_u32 v111, v111, v173, s19
	v_add3_u32 v113, v113, v175, s19
	v_add3_u32 v117, v117, v177, s19
	v_add3_u32 v115, v115, v181, s19
	v_add3_u32 v121, v121, v183, s19
	v_add3_u32 v119, v119, v185, s19
	v_lshrrev_b32_e32 v70, 16, v78
	v_lshrrev_b32_e32 v72, 16, v74
	v_lshrrev_b32_e32 v74, 16, v80
	v_lshrrev_b32_e32 v76, 16, v76
	v_lshrrev_b32_e32 v78, 16, v86
	v_lshrrev_b32_e32 v80, 16, v82
	v_lshrrev_b32_e32 v82, 16, v88
	v_lshrrev_b32_e32 v84, 16, v84
	v_lshrrev_b32_e32 v86, 16, v94
	v_lshrrev_b32_e32 v88, 16, v90
	v_lshrrev_b32_e32 v90, 16, v96
	v_lshrrev_b32_e32 v92, 16, v92
	v_lshrrev_b32_e32 v94, 16, v102
	v_lshrrev_b32_e32 v96, 16, v98
	v_lshrrev_b32_e32 v98, 16, v104
	v_lshrrev_b32_e32 v100, 16, v100
	v_lshrrev_b32_e32 v102, 16, v106
	v_lshrrev_b32_e32 v104, 16, v108
	v_lshrrev_b32_e32 v106, 16, v110
	v_lshrrev_b32_e32 v108, 16, v112
	v_lshrrev_b32_e32 v110, 16, v116
	v_lshrrev_b32_e32 v112, 16, v114
	v_lshrrev_b32_e32 v114, 16, v120
	v_lshrrev_b32_e32 v116, 16, v118
	v_and_or_b32 v194, v122, s18, v34
	v_and_or_b32 v195, v71, s18, v62
	v_and_or_b32 v196, v124, s18, v63
	v_and_or_b32 v197, v73, s18, v69
	v_and_or_b32 v198, v79, s18, v70
	v_and_or_b32 v199, v75, s18, v72
	v_and_or_b32 v200, v81, s18, v74
	v_and_or_b32 v201, v77, s18, v76
	v_and_or_b32 v202, v87, s18, v78
	v_and_or_b32 v203, v83, s18, v80
	v_and_or_b32 v204, v89, s18, v82
	v_and_or_b32 v205, v85, s18, v84
	v_and_or_b32 v206, v95, s18, v86
	v_and_or_b32 v207, v91, s18, v88
	v_and_or_b32 v208, v97, s18, v90
	v_and_or_b32 v209, v93, s18, v92
	v_and_or_b32 v210, v103, s18, v94
	v_and_or_b32 v211, v99, s18, v96
	v_and_or_b32 v212, v105, s18, v98
	v_and_or_b32 v213, v101, s18, v100
	v_and_or_b32 v214, v107, s18, v102
	v_and_or_b32 v215, v109, s18, v104
	v_and_or_b32 v216, v111, s18, v106
	v_and_or_b32 v217, v113, s18, v108
	v_and_or_b32 v218, v117, s18, v110
	v_and_or_b32 v219, v115, s18, v112
	v_and_or_b32 v220, v121, s18, v114
	v_and_or_b32 v221, v119, s18, v116
	v_mov_b32_e32 v246, v48
	v_mov_b32_e32 v247, v49
	v_mov_b32_e32 v248, v52
	v_mov_b32_e32 v249, v53
	v_mov_b32_e32 v250, v56
	v_mov_b32_e32 v251, v57
	v_mov_b32_e32 v252, v60
	v_mov_b32_e32 v253, v61
	s_cbranch_scc0 .Lmy_cv_loop
	global_store_dwordx4 v[246:247], v[190:193], off offset:-4096
	global_store_dwordx4 v[246:247], v[194:197], off
	global_store_dwordx4 v[248:249], v[198:201], off offset:-4096
	global_store_dwordx4 v[248:249], v[202:205], off
	global_store_dwordx4 v[250:251], v[206:209], off offset:-4096
	global_store_dwordx4 v[250:251], v[210:213], off
	global_store_dwordx4 v[252:253], v[214:217], off offset:-4096
	global_store_dwordx4 v[252:253], v[218:221], off
	s_add_i32 s22, s22, s34
	s_cmpk_gt_i32 s22, 0xff
	v_add_u32_e32 v64, s3, v64
	s_cbranch_scc0 .LBB0_1123
